# speedup vs baseline: 1.0149x; 1.0063x over previous
.LBB0_7:
	v_lshlrev_b32_e32 v0, 2, v0
	v_lshl_or_b32 v8, s3, 11, v0
	v_ashrrev_i32_e32 v9, 31, v8
	v_lshl_add_u64 v[4:5], v[8:9], 2, s[4:5]
	global_load_dwordx4 v[0:3], v[4:5], off nt
	v_add_co_u32_e32 v4, vcc, 0x1000, v4
	v_lshl_add_u64 v[8:9], v[8:9], 1, s[6:7]
	s_nop 0
	v_addc_co_u32_e32 v5, vcc, 0, v5, vcc
	global_load_dwordx4 v[4:7], v[4:5], off nt
	s_waitcnt vmcnt(1)
	v_cvt_pk_f16_f32 v3, v2, v3
	v_cvt_pk_f16_f32 v2, v0, v1
	s_waitcnt vmcnt(0)
	v_cvt_pk_f16_f32 v1, v6, v7
	v_cvt_pk_f16_f32 v0, v4, v5
	global_store_dwordx2 v[8:9], v[2:3], off sc1
	global_store_dwordx2 v[8:9], v[0:1], off offset:2048 sc1
	s_endpgm
